# speedup vs baseline: 1.0180x; 1.0165x over previous
_Z11center_mainPKfPKcS0_Pf:
	s_load_dwordx4 s[4:7], s[0:1], 0x0
	s_load_dwordx4 s[8:11], s[0:1], 0x10
	s_and_b32 s3, s2, 7
	s_lshr_b32 s12, s2, 3
	s_mov_b32 s30, s2
	v_lshrrev_b32_e32 v1, 6, v0
	v_and_b32_e32 v2, 63, v0
	v_bfe_u32 v3, v0, 3, 3
	v_and_b32_e32 v4, 7, v0
	v_lshrrev_b32_e32 v5, 7, v0
	v_bfe_u32 v6, v0, 6, 1
	v_lshl_or_b32 v7, v5, 3, v3
	v_lshlrev_b32_e32 v8, 10, v7
	v_lshl_or_b32 v8, v6, 9, v8
	v_lshl_or_b32 v226, v4, 4, v8
	v_lshlrev_b32_e32 v17, 15, v1
	v_lshl_or_b32 v227, v2, 5, v17
	v_lshlrev_b32_e32 v237, 3, v0
	s_lshl_b32 s13, s3, 22
	s_lshl_b32 s14, s12, 15
	s_add_u32 s13, s13, s14
	s_lshl_b32 s15, s3, 18
	s_lshl_b32 s28, s3, 12
	s_waitcnt lgkmcnt(0)
	s_add_u32 s16, s4, s13
	s_addc_u32 s17, s5, 0
	global_load_dwordx4 v[194:197], v226, s[16:17] offset:0 nt
	global_load_dwordx4 v[198:201], v226, s[16:17] offset:128 nt
	global_load_dwordx4 v[202:205], v226, s[16:17] offset:256 nt
	global_load_dwordx4 v[206:209], v226, s[16:17] offset:384 nt
	s_add_u32 s8, s8, s28
	s_addc_u32 s9, s9, 0
	global_load_dwordx2 v[238:239], v237, s[8:9]
	s_add_u32 s24, s6, s15
	s_addc_u32 s25, s7, 0
	s_add_u32 s32, s24, 0x1000
	s_addc_u32 s33, s25, 0
	s_add_u32 s34, s24, 0x2000
	s_addc_u32 s35, s25, 0
	s_add_u32 s36, s24, 0x3000
	s_addc_u32 s37, s25, 0
	s_add_u32 s38, s24, 0x4000
	s_addc_u32 s39, s25, 0
	s_add_u32 s40, s24, 0x5000
	s_addc_u32 s41, s25, 0
	s_add_u32 s42, s24, 0x6000
	s_addc_u32 s43, s25, 0
	s_add_u32 s44, s24, 0x7000
	s_addc_u32 s45, s25, 0
	global_load_dwordx4 v[34:37], v227, s[24:25] offset:0
	global_load_dwordx4 v[38:41], v227, s[24:25] offset:16
	global_load_dwordx4 v[26:29], v227, s[24:25] offset:2048
	global_load_dwordx4 v[30:33], v227, s[24:25] offset:2064
	global_load_dwordx4 v[50:53], v227, s[32:33] offset:0
	global_load_dwordx4 v[54:57], v227, s[32:33] offset:16
	global_load_dwordx4 v[42:45], v227, s[32:33] offset:2048
	global_load_dwordx4 v[46:49], v227, s[32:33] offset:2064
	global_load_dwordx4 v[18:21], v227, s[34:35] offset:0
	global_load_dwordx4 v[22:25], v227, s[34:35] offset:16
	global_load_dwordx4 v[130:133], v227, s[34:35] offset:2048
	global_load_dwordx4 v[134:137], v227, s[34:35] offset:2064
	global_load_dwordx4 v[122:125], v227, s[36:37] offset:0
	global_load_dwordx4 v[126:129], v227, s[36:37] offset:16
	global_load_dwordx4 v[138:141], v227, s[36:37] offset:2048
	global_load_dwordx4 v[142:145], v227, s[36:37] offset:2064
	global_load_dwordx4 v[98:101], v227, s[38:39] offset:0
	global_load_dwordx4 v[102:105], v227, s[38:39] offset:16
	global_load_dwordx4 v[90:93], v227, s[38:39] offset:2048
	global_load_dwordx4 v[94:97], v227, s[38:39] offset:2064
	global_load_dwordx4 v[114:117], v227, s[40:41] offset:0
	global_load_dwordx4 v[118:121], v227, s[40:41] offset:16
	global_load_dwordx4 v[106:109], v227, s[40:41] offset:2048
	global_load_dwordx4 v[110:113], v227, s[40:41] offset:2064
	global_load_dwordx4 v[58:61], v227, s[42:43] offset:0
	global_load_dwordx4 v[62:65], v227, s[42:43] offset:16
	global_load_dwordx4 v[66:69], v227, s[42:43] offset:2048
	global_load_dwordx4 v[70:73], v227, s[42:43] offset:2064
	global_load_dwordx4 v[74:77], v227, s[44:45] offset:0
	global_load_dwordx4 v[78:81], v227, s[44:45] offset:16
	global_load_dwordx4 v[82:85], v227, s[44:45] offset:2048
	global_load_dwordx4 v[86:89], v227, s[44:45] offset:2064
	s_add_u32 s18, s16, 0x100000
	s_addc_u32 s19, s17, 0
	s_add_u32 s20, s16, 0x200000
	s_addc_u32 s21, s17, 0
	s_add_u32 s22, s16, 0x300000
	s_addc_u32 s23, s17, 0
	v_mul_u32_u24_e32 v9, 0x110, v7
	v_lshl_add_u32 v9, v6, 7, v9
	v_lshl_add_u32 v228, v4, 4, v9
	v_lshlrev_b32_e32 v10, 6, v7
	v_lshl_or_b32 v10, v6, 5, v10
	v_lshl_or_b32 v229, v4, 2, v10
	v_and_b32_e32 v11, 31, v0
	v_bfe_u32 v12, v0, 5, 1
	v_mul_u32_u24_e32 v13, 0x110, v11
	v_lshl_add_u32 v230, v12, 5, v13
	v_lshlrev_b32_e32 v14, 9, v1
	v_lshl_or_b32 v231, v12, 4, v14
	v_xor_b32_e32 v15, 32, v2
	v_lshlrev_b32_e32 v232, 2, v15
	v_xor_b32_e32 v15, 16, v2
	v_lshlrev_b32_e32 v247, 2, v15
	v_lshlrev_b32_e32 v16, 7, v1
	v_lshl_or_b32 v233, v11, 2, v16
	v_mov_b32_e32 v234, 0x7f7f7f7f
	s_waitcnt vmcnt(32)
	ds_write_b64 v237, v[238:239] offset:34816
	v_mul_f32_e32 v244, v194, v194
	v_mul_f32_e32 v245, v198, v198
	v_cvt_pk_fp8_f32 v240, v194, v195
	v_cvt_pk_fp8_f32 v241, v198, v199
	v_cvt_pk_fp8_f32 v242, v202, v203
	v_cvt_pk_fp8_f32 v243, v206, v207
	v_fmac_f32_e32 v244, v195, v195
	v_fmac_f32_e32 v245, v199, v199
	v_fmac_f32_e32 v244, v196, v196
	v_fmac_f32_e32 v245, v200, v200
	v_fmac_f32_e32 v244, v197, v197
	v_fmac_f32_e32 v245, v201, v201
	v_fmac_f32_e32 v244, v202, v202
	v_fmac_f32_e32 v245, v206, v206
	v_fmac_f32_e32 v244, v203, v203
	v_fmac_f32_e32 v245, v207, v207
	v_fmac_f32_e32 v244, v204, v204
	v_fmac_f32_e32 v245, v208, v208
	v_fmac_f32_e32 v244, v205, v205
	v_fmac_f32_e32 v245, v209, v209
	v_cvt_pk_fp8_f32 v240, v196, v197 op_sel:[0,0,1]
	v_cvt_pk_fp8_f32 v241, v200, v201 op_sel:[0,0,1]
	v_cvt_pk_fp8_f32 v242, v204, v205 op_sel:[0,0,1]
	v_cvt_pk_fp8_f32 v243, v208, v209 op_sel:[0,0,1]
	v_add_f32_e32 v244, v244, v245
	s_nop 0
	ds_write_b128 v228, v[240:243] offset:0
	ds_write_b32 v229, v244 offset:38912
	global_load_dwordx4 v[210:213], v226, s[18:19] offset:0 nt
	global_load_dwordx4 v[214:217], v226, s[18:19] offset:128 nt
	global_load_dwordx4 v[218:221], v226, s[18:19] offset:256 nt
	global_load_dwordx4 v[222:225], v226, s[18:19] offset:384 nt
	s_waitcnt lgkmcnt(0)
	s_barrier
	ds_read_b128 v[162:165], v230 offset:0
	ds_read_b128 v[166:169], v230 offset:16
	ds_read_b128 v[2:5], v231 offset:34816
	ds_read_b128 v[6:9], v231 offset:34848
	ds_read_b128 v[10:13], v231 offset:34880
	ds_read_b128 v[14:17], v231 offset:34912
	ds_read_b128 v[170:173], v230 offset:64
	ds_read_b128 v[174:177], v230 offset:80
	ds_read_b128 v[178:181], v230 offset:128
	ds_read_b128 v[182:185], v230 offset:144
	ds_read_b128 v[186:189], v230 offset:192
	ds_read_b128 v[190:193], v230 offset:208
	s_waitcnt vmcnt(34) lgkmcnt(6)
	v_mfma_scale_f32_32x32x64_f8f6f4 v[2:17], v[34:41], v[162:169], v[2:17], v234, v234 op_sel_hi:[0,0,0]
	s_waitcnt vmcnt(32) lgkmcnt(4)
	v_mfma_scale_f32_32x32x64_f8f6f4 v[2:17], v[26:33], v[170:177], v[2:17], v234, v234 op_sel_hi:[0,0,0]
	s_waitcnt vmcnt(30) lgkmcnt(2)
	v_mfma_scale_f32_32x32x64_f8f6f4 v[2:17], v[50:57], v[178:185], v[2:17], v234, v234 op_sel_hi:[0,0,0]
	s_waitcnt vmcnt(28) lgkmcnt(0)
	v_mfma_scale_f32_32x32x64_f8f6f4 v[2:17], v[42:49], v[186:193], v[2:17], v234, v234 op_sel_hi:[0,0,0]
	ds_read_b128 v[146:149], v231 offset:34944
	ds_read_b128 v[150:153], v231 offset:34976
	ds_read_b128 v[154:157], v231 offset:35008
	ds_read_b128 v[158:161], v231 offset:35040
	s_waitcnt vmcnt(26) lgkmcnt(0)
	v_mfma_scale_f32_32x32x64_f8f6f4 v[146:161], v[18:25], v[162:169], v[146:161], v234, v234 op_sel_hi:[0,0,0]
	s_waitcnt vmcnt(24)
	v_mfma_scale_f32_32x32x64_f8f6f4 v[146:161], v[130:137], v[170:177], v[146:161], v234, v234 op_sel_hi:[0,0,0]
	s_waitcnt vmcnt(22)
	v_mfma_scale_f32_32x32x64_f8f6f4 v[146:161], v[122:129], v[178:185], v[146:161], v234, v234 op_sel_hi:[0,0,0]
	s_waitcnt vmcnt(20)
	v_mfma_scale_f32_32x32x64_f8f6f4 v[146:161], v[138:145], v[186:193], v[146:161], v234, v234 op_sel_hi:[0,0,0]
	v_min3_f32 v2, v2, v3, v4
	v_min3_f32 v5, v5, v6, v7
	v_min3_f32 v8, v8, v9, v10
	v_min3_f32 v11, v11, v12, v13
	v_min3_f32 v14, v14, v15, v16
	v_min3_f32 v2, v2, v5, v8
	v_min3_f32 v11, v11, v14, v17
	v_min_f32_e32 v235, v2, v11
	ds_read_b128 v[2:5], v231 offset:35072
	ds_read_b128 v[6:9], v231 offset:35104
	ds_read_b128 v[10:13], v231 offset:35136
	ds_read_b128 v[14:17], v231 offset:35168
	s_waitcnt vmcnt(18) lgkmcnt(0)
	v_mfma_scale_f32_32x32x64_f8f6f4 v[2:17], v[98:105], v[162:169], v[2:17], v234, v234 op_sel_hi:[0,0,0]
	s_waitcnt vmcnt(16)
	v_mfma_scale_f32_32x32x64_f8f6f4 v[2:17], v[90:97], v[170:177], v[2:17], v234, v234 op_sel_hi:[0,0,0]
	s_waitcnt vmcnt(14)
	v_mfma_scale_f32_32x32x64_f8f6f4 v[2:17], v[114:121], v[178:185], v[2:17], v234, v234 op_sel_hi:[0,0,0]
	s_waitcnt vmcnt(12)
	v_mfma_scale_f32_32x32x64_f8f6f4 v[2:17], v[106:113], v[186:193], v[2:17], v234, v234 op_sel_hi:[0,0,0]
	v_min3_f32 v146, v146, v147, v148
	v_min3_f32 v149, v149, v150, v151
	v_min3_f32 v152, v152, v153, v154
	v_min3_f32 v155, v155, v156, v157
	v_min3_f32 v158, v158, v159, v160
	v_min3_f32 v146, v146, v149, v152
	v_min3_f32 v155, v155, v158, v161
	v_min3_f32 v235, v235, v146, v155
	ds_read_b128 v[146:149], v231 offset:35200
	ds_read_b128 v[150:153], v231 offset:35232
	ds_read_b128 v[154:157], v231 offset:35264
	ds_read_b128 v[158:161], v231 offset:35296
	s_waitcnt vmcnt(10) lgkmcnt(0)
	v_mfma_scale_f32_32x32x64_f8f6f4 v[146:161], v[58:65], v[162:169], v[146:161], v234, v234 op_sel_hi:[0,0,0]
	s_waitcnt vmcnt(8)
	v_mfma_scale_f32_32x32x64_f8f6f4 v[146:161], v[66:73], v[170:177], v[146:161], v234, v234 op_sel_hi:[0,0,0]
	s_waitcnt vmcnt(6)
	v_mfma_scale_f32_32x32x64_f8f6f4 v[146:161], v[74:81], v[178:185], v[146:161], v234, v234 op_sel_hi:[0,0,0]
	s_waitcnt vmcnt(4)
	v_mfma_scale_f32_32x32x64_f8f6f4 v[146:161], v[82:89], v[186:193], v[146:161], v234, v234 op_sel_hi:[0,0,0]
	global_load_dwordx4 v[194:197], v226, s[20:21] offset:0 nt
	global_load_dwordx4 v[198:201], v226, s[20:21] offset:128 nt
	global_load_dwordx4 v[202:205], v226, s[20:21] offset:256 nt
	global_load_dwordx4 v[206:209], v226, s[20:21] offset:384 nt
	s_waitcnt vmcnt(4)
	v_mul_f32_e32 v244, v210, v210
	v_mul_f32_e32 v245, v214, v214
	v_cvt_pk_fp8_f32 v240, v210, v211
	v_cvt_pk_fp8_f32 v241, v214, v215
	v_cvt_pk_fp8_f32 v242, v218, v219
	v_cvt_pk_fp8_f32 v243, v222, v223
	v_fmac_f32_e32 v244, v211, v211
	v_fmac_f32_e32 v245, v215, v215
	v_fmac_f32_e32 v244, v212, v212
	v_fmac_f32_e32 v245, v216, v216
	v_fmac_f32_e32 v244, v213, v213
	v_fmac_f32_e32 v245, v217, v217
	v_fmac_f32_e32 v244, v218, v218
	v_fmac_f32_e32 v245, v222, v222
	v_fmac_f32_e32 v244, v219, v219
	v_fmac_f32_e32 v245, v223, v223
	v_fmac_f32_e32 v244, v220, v220
	v_fmac_f32_e32 v245, v224, v224
	v_fmac_f32_e32 v244, v221, v221
	v_fmac_f32_e32 v245, v225, v225
	v_cvt_pk_fp8_f32 v240, v212, v213 op_sel:[0,0,1]
	v_cvt_pk_fp8_f32 v241, v216, v217 op_sel:[0,0,1]
	v_cvt_pk_fp8_f32 v242, v220, v221 op_sel:[0,0,1]
	v_cvt_pk_fp8_f32 v243, v224, v225 op_sel:[0,0,1]
	v_add_f32_e32 v244, v244, v245
	s_nop 0
	ds_write_b128 v228, v[240:243] offset:8704
	ds_write_b32 v229, v244 offset:40960
	v_min3_f32 v2, v2, v3, v4
	v_min3_f32 v5, v5, v6, v7
	v_min3_f32 v8, v8, v9, v10
	v_min3_f32 v11, v11, v12, v13
	v_min3_f32 v14, v14, v15, v16
	v_min3_f32 v2, v2, v5, v8
	v_min3_f32 v11, v11, v14, v17
	v_min3_f32 v235, v235, v2, v11
	ds_read_b128 v[2:5], v231 offset:34816
	ds_read_b128 v[6:9], v231 offset:34848
	ds_read_b128 v[10:13], v231 offset:34880
	ds_read_b128 v[14:17], v231 offset:34912
	s_waitcnt lgkmcnt(0)
	s_barrier
	ds_read_b128 v[162:165], v230 offset:8704
	ds_read_b128 v[166:169], v230 offset:8720
	ds_read_b128 v[170:173], v230 offset:8768
	ds_read_b128 v[174:177], v230 offset:8784
	ds_read_b128 v[178:181], v230 offset:8832
	ds_read_b128 v[182:185], v230 offset:8848
	ds_read_b128 v[186:189], v230 offset:8896
	ds_read_b128 v[190:193], v230 offset:8912
	s_waitcnt lgkmcnt(6)
	v_mfma_scale_f32_32x32x64_f8f6f4 v[2:17], v[34:41], v[162:169], v[2:17], v234, v234 op_sel_hi:[0,0,0]
	s_waitcnt lgkmcnt(4)
	v_mfma_scale_f32_32x32x64_f8f6f4 v[2:17], v[26:33], v[170:177], v[2:17], v234, v234 op_sel_hi:[0,0,0]
	s_waitcnt lgkmcnt(2)
	v_mfma_scale_f32_32x32x64_f8f6f4 v[2:17], v[50:57], v[178:185], v[2:17], v234, v234 op_sel_hi:[0,0,0]
	s_waitcnt lgkmcnt(0)
	v_mfma_scale_f32_32x32x64_f8f6f4 v[2:17], v[42:49], v[186:193], v[2:17], v234, v234 op_sel_hi:[0,0,0]
	v_min3_f32 v146, v146, v147, v148
	v_min3_f32 v149, v149, v150, v151
	v_min3_f32 v152, v152, v153, v154
	v_min3_f32 v155, v155, v156, v157
	v_min3_f32 v158, v158, v159, v160
	v_min3_f32 v146, v146, v149, v152
	v_min3_f32 v155, v155, v158, v161
	v_min3_f32 v235, v235, v146, v155
	ds_bpermute_b32 v246, v232, v235
	s_waitcnt lgkmcnt(0)
	v_min_f32_e32 v246, v235, v246
	ds_write_b32 v233, v246 offset:47104
	ds_read_b128 v[146:149], v231 offset:34944
	ds_read_b128 v[150:153], v231 offset:34976
	ds_read_b128 v[154:157], v231 offset:35008
	ds_read_b128 v[158:161], v231 offset:35040
	s_waitcnt lgkmcnt(0)
	v_mfma_scale_f32_32x32x64_f8f6f4 v[146:161], v[18:25], v[162:169], v[146:161], v234, v234 op_sel_hi:[0,0,0]
	v_mfma_scale_f32_32x32x64_f8f6f4 v[146:161], v[130:137], v[170:177], v[146:161], v234, v234 op_sel_hi:[0,0,0]
	v_mfma_scale_f32_32x32x64_f8f6f4 v[146:161], v[122:129], v[178:185], v[146:161], v234, v234 op_sel_hi:[0,0,0]
	v_mfma_scale_f32_32x32x64_f8f6f4 v[146:161], v[138:145], v[186:193], v[146:161], v234, v234 op_sel_hi:[0,0,0]
	v_min3_f32 v2, v2, v3, v4
	v_min3_f32 v5, v5, v6, v7
	v_min3_f32 v8, v8, v9, v10
	v_min3_f32 v11, v11, v12, v13
	v_min3_f32 v14, v14, v15, v16
	v_min3_f32 v2, v2, v5, v8
	v_min3_f32 v11, v11, v14, v17
	v_min_f32_e32 v236, v2, v11
	ds_read_b128 v[2:5], v231 offset:35072
	ds_read_b128 v[6:9], v231 offset:35104
	ds_read_b128 v[10:13], v231 offset:35136
	ds_read_b128 v[14:17], v231 offset:35168
	s_waitcnt lgkmcnt(0)
	v_mfma_scale_f32_32x32x64_f8f6f4 v[2:17], v[98:105], v[162:169], v[2:17], v234, v234 op_sel_hi:[0,0,0]
	v_mfma_scale_f32_32x32x64_f8f6f4 v[2:17], v[90:97], v[170:177], v[2:17], v234, v234 op_sel_hi:[0,0,0]
	v_mfma_scale_f32_32x32x64_f8f6f4 v[2:17], v[114:121], v[178:185], v[2:17], v234, v234 op_sel_hi:[0,0,0]
	v_mfma_scale_f32_32x32x64_f8f6f4 v[2:17], v[106:113], v[186:193], v[2:17], v234, v234 op_sel_hi:[0,0,0]
	v_min3_f32 v146, v146, v147, v148
	v_min3_f32 v149, v149, v150, v151
	v_min3_f32 v152, v152, v153, v154
	v_min3_f32 v155, v155, v156, v157
	v_min3_f32 v158, v158, v159, v160
	v_min3_f32 v146, v146, v149, v152
	v_min3_f32 v155, v155, v158, v161
	v_min3_f32 v236, v236, v146, v155
	ds_read_b128 v[146:149], v231 offset:35200
	ds_read_b128 v[150:153], v231 offset:35232
	ds_read_b128 v[154:157], v231 offset:35264
	ds_read_b128 v[158:161], v231 offset:35296
	s_waitcnt lgkmcnt(0)
	v_mfma_scale_f32_32x32x64_f8f6f4 v[146:161], v[58:65], v[162:169], v[146:161], v234, v234 op_sel_hi:[0,0,0]
	v_mfma_scale_f32_32x32x64_f8f6f4 v[146:161], v[66:73], v[170:177], v[146:161], v234, v234 op_sel_hi:[0,0,0]
	v_mfma_scale_f32_32x32x64_f8f6f4 v[146:161], v[74:81], v[178:185], v[146:161], v234, v234 op_sel_hi:[0,0,0]
	v_mfma_scale_f32_32x32x64_f8f6f4 v[146:161], v[82:89], v[186:193], v[146:161], v234, v234 op_sel_hi:[0,0,0]
	global_load_dwordx4 v[210:213], v226, s[22:23] offset:0 nt
	global_load_dwordx4 v[214:217], v226, s[22:23] offset:128 nt
	global_load_dwordx4 v[218:221], v226, s[22:23] offset:256 nt
	global_load_dwordx4 v[222:225], v226, s[22:23] offset:384 nt
	s_waitcnt vmcnt(4)
	v_mul_f32_e32 v244, v194, v194
	v_mul_f32_e32 v245, v198, v198
	v_cvt_pk_fp8_f32 v240, v194, v195
	v_cvt_pk_fp8_f32 v241, v198, v199
	v_cvt_pk_fp8_f32 v242, v202, v203
	v_cvt_pk_fp8_f32 v243, v206, v207
	v_fmac_f32_e32 v244, v195, v195
	v_fmac_f32_e32 v245, v199, v199
	v_fmac_f32_e32 v244, v196, v196
	v_fmac_f32_e32 v245, v200, v200
	v_fmac_f32_e32 v244, v197, v197
	v_fmac_f32_e32 v245, v201, v201
	v_fmac_f32_e32 v244, v202, v202
	v_fmac_f32_e32 v245, v206, v206
	v_fmac_f32_e32 v244, v203, v203
	v_fmac_f32_e32 v245, v207, v207
	v_fmac_f32_e32 v244, v204, v204
	v_fmac_f32_e32 v245, v208, v208
	v_fmac_f32_e32 v244, v205, v205
	v_fmac_f32_e32 v245, v209, v209
	v_cvt_pk_fp8_f32 v240, v196, v197 op_sel:[0,0,1]
	v_cvt_pk_fp8_f32 v241, v200, v201 op_sel:[0,0,1]
	v_cvt_pk_fp8_f32 v242, v204, v205 op_sel:[0,0,1]
	v_cvt_pk_fp8_f32 v243, v208, v209 op_sel:[0,0,1]
	v_add_f32_e32 v244, v244, v245
	s_nop 0
	ds_write_b128 v228, v[240:243] offset:17408
	ds_write_b32 v229, v244 offset:43008
	v_min3_f32 v2, v2, v3, v4
	v_min3_f32 v5, v5, v6, v7
	v_min3_f32 v8, v8, v9, v10
	v_min3_f32 v11, v11, v12, v13
	v_min3_f32 v14, v14, v15, v16
	v_min3_f32 v2, v2, v5, v8
	v_min3_f32 v11, v11, v14, v17
	v_min3_f32 v236, v236, v2, v11
	ds_read_b128 v[2:5], v231 offset:34816
	ds_read_b128 v[6:9], v231 offset:34848
	ds_read_b128 v[10:13], v231 offset:34880
	ds_read_b128 v[14:17], v231 offset:34912
	s_waitcnt lgkmcnt(0)
	s_barrier
	ds_read_b128 v[162:165], v230 offset:17408
	ds_read_b128 v[166:169], v230 offset:17424
	ds_read_b128 v[170:173], v230 offset:17472
	ds_read_b128 v[174:177], v230 offset:17488
	ds_read_b128 v[178:181], v230 offset:17536
	ds_read_b128 v[182:185], v230 offset:17552
	ds_read_b128 v[186:189], v230 offset:17600
	ds_read_b128 v[190:193], v230 offset:17616
	s_waitcnt lgkmcnt(6)
	v_mfma_scale_f32_32x32x64_f8f6f4 v[2:17], v[34:41], v[162:169], v[2:17], v234, v234 op_sel_hi:[0,0,0]
	s_waitcnt lgkmcnt(4)
	v_mfma_scale_f32_32x32x64_f8f6f4 v[2:17], v[26:33], v[170:177], v[2:17], v234, v234 op_sel_hi:[0,0,0]
	s_waitcnt lgkmcnt(2)
	v_mfma_scale_f32_32x32x64_f8f6f4 v[2:17], v[50:57], v[178:185], v[2:17], v234, v234 op_sel_hi:[0,0,0]
	s_waitcnt lgkmcnt(0)
	v_mfma_scale_f32_32x32x64_f8f6f4 v[2:17], v[42:49], v[186:193], v[2:17], v234, v234 op_sel_hi:[0,0,0]
	v_min3_f32 v146, v146, v147, v148
	v_min3_f32 v149, v149, v150, v151
	v_min3_f32 v152, v152, v153, v154
	v_min3_f32 v155, v155, v156, v157
	v_min3_f32 v158, v158, v159, v160
	v_min3_f32 v146, v146, v149, v152
	v_min3_f32 v155, v155, v158, v161
	v_min3_f32 v236, v236, v146, v155
	ds_bpermute_b32 v246, v232, v236
	s_waitcnt lgkmcnt(0)
	v_min_f32_e32 v246, v236, v246
	ds_write_b32 v233, v246 offset:48128
	ds_read_b128 v[146:149], v231 offset:34944
	ds_read_b128 v[150:153], v231 offset:34976
	ds_read_b128 v[154:157], v231 offset:35008
	ds_read_b128 v[158:161], v231 offset:35040
	s_waitcnt lgkmcnt(0)
	v_mfma_scale_f32_32x32x64_f8f6f4 v[146:161], v[18:25], v[162:169], v[146:161], v234, v234 op_sel_hi:[0,0,0]
	v_mfma_scale_f32_32x32x64_f8f6f4 v[146:161], v[130:137], v[170:177], v[146:161], v234, v234 op_sel_hi:[0,0,0]
	v_mfma_scale_f32_32x32x64_f8f6f4 v[146:161], v[122:129], v[178:185], v[146:161], v234, v234 op_sel_hi:[0,0,0]
	v_mfma_scale_f32_32x32x64_f8f6f4 v[146:161], v[138:145], v[186:193], v[146:161], v234, v234 op_sel_hi:[0,0,0]
	v_min3_f32 v2, v2, v3, v4
	v_min3_f32 v5, v5, v6, v7
	v_min3_f32 v8, v8, v9, v10
	v_min3_f32 v11, v11, v12, v13
	v_min3_f32 v14, v14, v15, v16
	v_min3_f32 v2, v2, v5, v8
	v_min3_f32 v11, v11, v14, v17
	v_min_f32_e32 v235, v2, v11
	ds_read_b128 v[2:5], v231 offset:35072
	ds_read_b128 v[6:9], v231 offset:35104
	ds_read_b128 v[10:13], v231 offset:35136
	ds_read_b128 v[14:17], v231 offset:35168
	s_waitcnt lgkmcnt(0)
	v_mfma_scale_f32_32x32x64_f8f6f4 v[2:17], v[98:105], v[162:169], v[2:17], v234, v234 op_sel_hi:[0,0,0]
	v_mfma_scale_f32_32x32x64_f8f6f4 v[2:17], v[90:97], v[170:177], v[2:17], v234, v234 op_sel_hi:[0,0,0]
	v_mfma_scale_f32_32x32x64_f8f6f4 v[2:17], v[114:121], v[178:185], v[2:17], v234, v234 op_sel_hi:[0,0,0]
	v_mfma_scale_f32_32x32x64_f8f6f4 v[2:17], v[106:113], v[186:193], v[2:17], v234, v234 op_sel_hi:[0,0,0]
	v_min3_f32 v146, v146, v147, v148
	v_min3_f32 v149, v149, v150, v151
	v_min3_f32 v152, v152, v153, v154
	v_min3_f32 v155, v155, v156, v157
	v_min3_f32 v158, v158, v159, v160
	v_min3_f32 v146, v146, v149, v152
	v_min3_f32 v155, v155, v158, v161
	v_min3_f32 v235, v235, v146, v155
	ds_read_b128 v[146:149], v231 offset:35200
	ds_read_b128 v[150:153], v231 offset:35232
	ds_read_b128 v[154:157], v231 offset:35264
	ds_read_b128 v[158:161], v231 offset:35296
	s_waitcnt lgkmcnt(0)
	v_mfma_scale_f32_32x32x64_f8f6f4 v[146:161], v[58:65], v[162:169], v[146:161], v234, v234 op_sel_hi:[0,0,0]
	v_mfma_scale_f32_32x32x64_f8f6f4 v[146:161], v[66:73], v[170:177], v[146:161], v234, v234 op_sel_hi:[0,0,0]
	v_mfma_scale_f32_32x32x64_f8f6f4 v[146:161], v[74:81], v[178:185], v[146:161], v234, v234 op_sel_hi:[0,0,0]
	v_mfma_scale_f32_32x32x64_f8f6f4 v[146:161], v[82:89], v[186:193], v[146:161], v234, v234 op_sel_hi:[0,0,0]
	s_waitcnt vmcnt(0)
	v_mul_f32_e32 v244, v210, v210
	v_mul_f32_e32 v245, v214, v214
	v_cvt_pk_fp8_f32 v240, v210, v211
	v_cvt_pk_fp8_f32 v241, v214, v215
	v_cvt_pk_fp8_f32 v242, v218, v219
	v_cvt_pk_fp8_f32 v243, v222, v223
	v_fmac_f32_e32 v244, v211, v211
	v_fmac_f32_e32 v245, v215, v215
	v_fmac_f32_e32 v244, v212, v212
	v_fmac_f32_e32 v245, v216, v216
	v_fmac_f32_e32 v244, v213, v213
	v_fmac_f32_e32 v245, v217, v217
	v_fmac_f32_e32 v244, v218, v218
	v_fmac_f32_e32 v245, v222, v222
	v_fmac_f32_e32 v244, v219, v219
	v_fmac_f32_e32 v245, v223, v223
	v_fmac_f32_e32 v244, v220, v220
	v_fmac_f32_e32 v245, v224, v224
	v_fmac_f32_e32 v244, v221, v221
	v_fmac_f32_e32 v245, v225, v225
	v_cvt_pk_fp8_f32 v240, v212, v213 op_sel:[0,0,1]
	v_cvt_pk_fp8_f32 v241, v216, v217 op_sel:[0,0,1]
	v_cvt_pk_fp8_f32 v242, v220, v221 op_sel:[0,0,1]
	v_cvt_pk_fp8_f32 v243, v224, v225 op_sel:[0,0,1]
	v_add_f32_e32 v244, v244, v245
	s_nop 0
	ds_write_b128 v228, v[240:243] offset:26112
	ds_write_b32 v229, v244 offset:45056
	v_min3_f32 v2, v2, v3, v4
	v_min3_f32 v5, v5, v6, v7
	v_min3_f32 v8, v8, v9, v10
	v_min3_f32 v11, v11, v12, v13
	v_min3_f32 v14, v14, v15, v16
	v_min3_f32 v2, v2, v5, v8
	v_min3_f32 v11, v11, v14, v17
	v_min3_f32 v235, v235, v2, v11
	ds_read_b128 v[2:5], v231 offset:34816
	ds_read_b128 v[6:9], v231 offset:34848
	ds_read_b128 v[10:13], v231 offset:34880
	ds_read_b128 v[14:17], v231 offset:34912
	s_waitcnt lgkmcnt(0)
	s_barrier
	ds_read_b128 v[162:165], v230 offset:26112
	ds_read_b128 v[166:169], v230 offset:26128
	ds_read_b128 v[170:173], v230 offset:26176
	ds_read_b128 v[174:177], v230 offset:26192
	ds_read_b128 v[178:181], v230 offset:26240
	ds_read_b128 v[182:185], v230 offset:26256
	ds_read_b128 v[186:189], v230 offset:26304
	ds_read_b128 v[190:193], v230 offset:26320
	s_waitcnt lgkmcnt(6)
	v_mfma_scale_f32_32x32x64_f8f6f4 v[2:17], v[34:41], v[162:169], v[2:17], v234, v234 op_sel_hi:[0,0,0]
	s_waitcnt lgkmcnt(4)
	v_mfma_scale_f32_32x32x64_f8f6f4 v[2:17], v[26:33], v[170:177], v[2:17], v234, v234 op_sel_hi:[0,0,0]
	s_waitcnt lgkmcnt(2)
	v_mfma_scale_f32_32x32x64_f8f6f4 v[2:17], v[50:57], v[178:185], v[2:17], v234, v234 op_sel_hi:[0,0,0]
	s_waitcnt lgkmcnt(0)
	v_mfma_scale_f32_32x32x64_f8f6f4 v[2:17], v[42:49], v[186:193], v[2:17], v234, v234 op_sel_hi:[0,0,0]
	v_min3_f32 v146, v146, v147, v148
	v_min3_f32 v149, v149, v150, v151
	v_min3_f32 v152, v152, v153, v154
	v_min3_f32 v155, v155, v156, v157
	v_min3_f32 v158, v158, v159, v160
	v_min3_f32 v146, v146, v149, v152
	v_min3_f32 v155, v155, v158, v161
	v_min3_f32 v235, v235, v146, v155
	ds_bpermute_b32 v246, v232, v235
	s_waitcnt lgkmcnt(0)
	v_min_f32_e32 v246, v235, v246
	ds_write_b32 v233, v246 offset:49152
	ds_read_b128 v[146:149], v231 offset:34944
	ds_read_b128 v[150:153], v231 offset:34976
	ds_read_b128 v[154:157], v231 offset:35008
	ds_read_b128 v[158:161], v231 offset:35040
	s_waitcnt lgkmcnt(0)
	v_mfma_scale_f32_32x32x64_f8f6f4 v[146:161], v[18:25], v[162:169], v[146:161], v234, v234 op_sel_hi:[0,0,0]
	v_mfma_scale_f32_32x32x64_f8f6f4 v[146:161], v[130:137], v[170:177], v[146:161], v234, v234 op_sel_hi:[0,0,0]
	v_mfma_scale_f32_32x32x64_f8f6f4 v[146:161], v[122:129], v[178:185], v[146:161], v234, v234 op_sel_hi:[0,0,0]
	v_mfma_scale_f32_32x32x64_f8f6f4 v[146:161], v[138:145], v[186:193], v[146:161], v234, v234 op_sel_hi:[0,0,0]
	v_min3_f32 v2, v2, v3, v4
	v_min3_f32 v5, v5, v6, v7
	v_min3_f32 v8, v8, v9, v10
	v_min3_f32 v11, v11, v12, v13
	v_min3_f32 v14, v14, v15, v16
	v_min3_f32 v2, v2, v5, v8
	v_min3_f32 v11, v11, v14, v17
	v_min_f32_e32 v236, v2, v11
	ds_read_b128 v[2:5], v231 offset:35072
	ds_read_b128 v[6:9], v231 offset:35104
	ds_read_b128 v[10:13], v231 offset:35136
	ds_read_b128 v[14:17], v231 offset:35168
	s_waitcnt lgkmcnt(0)
	v_mfma_scale_f32_32x32x64_f8f6f4 v[2:17], v[98:105], v[162:169], v[2:17], v234, v234 op_sel_hi:[0,0,0]
	v_mfma_scale_f32_32x32x64_f8f6f4 v[2:17], v[90:97], v[170:177], v[2:17], v234, v234 op_sel_hi:[0,0,0]
	v_mfma_scale_f32_32x32x64_f8f6f4 v[2:17], v[114:121], v[178:185], v[2:17], v234, v234 op_sel_hi:[0,0,0]
	v_mfma_scale_f32_32x32x64_f8f6f4 v[2:17], v[106:113], v[186:193], v[2:17], v234, v234 op_sel_hi:[0,0,0]
	v_min3_f32 v146, v146, v147, v148
	v_min3_f32 v149, v149, v150, v151
	v_min3_f32 v152, v152, v153, v154
	v_min3_f32 v155, v155, v156, v157
	v_min3_f32 v158, v158, v159, v160
	v_min3_f32 v146, v146, v149, v152
	v_min3_f32 v155, v155, v158, v161
	v_min3_f32 v236, v236, v146, v155
	ds_read_b128 v[146:149], v231 offset:35200
	ds_read_b128 v[150:153], v231 offset:35232
	ds_read_b128 v[154:157], v231 offset:35264
	ds_read_b128 v[158:161], v231 offset:35296
	s_waitcnt lgkmcnt(0)
	v_mfma_scale_f32_32x32x64_f8f6f4 v[146:161], v[58:65], v[162:169], v[146:161], v234, v234 op_sel_hi:[0,0,0]
	v_mfma_scale_f32_32x32x64_f8f6f4 v[146:161], v[66:73], v[170:177], v[146:161], v234, v234 op_sel_hi:[0,0,0]
	v_mfma_scale_f32_32x32x64_f8f6f4 v[146:161], v[74:81], v[178:185], v[146:161], v234, v234 op_sel_hi:[0,0,0]
	v_mfma_scale_f32_32x32x64_f8f6f4 v[146:161], v[82:89], v[186:193], v[146:161], v234, v234 op_sel_hi:[0,0,0]
	v_cmp_gt_u32_e32 vcc, 0x80, v0
	s_and_saveexec_b64 s[34:35], vcc
	v_lshlrev_b32_e32 v36, 6, v0
	ds_read_b128 v[20:23], v36 offset:38912
	ds_read_b128 v[24:27], v36 offset:38928
	ds_read_b128 v[28:31], v36 offset:38944
	ds_read_b128 v[32:35], v36 offset:38960
	s_mov_b64 exec, s[34:35]
	v_min3_f32 v2, v2, v3, v4
	v_min3_f32 v5, v5, v6, v7
	v_min3_f32 v8, v8, v9, v10
	v_min3_f32 v11, v11, v12, v13
	v_min3_f32 v14, v14, v15, v16
	v_min3_f32 v2, v2, v5, v8
	v_min3_f32 v11, v11, v14, v17
	v_min3_f32 v236, v236, v2, v11
	s_nop 15
	v_min3_f32 v146, v146, v147, v148
	v_min3_f32 v149, v149, v150, v151
	v_min3_f32 v152, v152, v153, v154
	v_min3_f32 v155, v155, v156, v157
	v_min3_f32 v158, v158, v159, v160
	v_min3_f32 v146, v146, v149, v152
	v_min3_f32 v155, v155, v158, v161
	v_min3_f32 v236, v236, v146, v155
	ds_bpermute_b32 v246, v232, v236
	s_waitcnt lgkmcnt(0)
	v_min_f32_e32 v246, v236, v246
	ds_write_b32 v233, v246 offset:50176
	s_waitcnt lgkmcnt(0)
	s_barrier
	v_readfirstlane_b32 s2, v1
	s_nop 3
	s_cmp_gt_u32 s2, 1
	s_cbranch_scc1 .Lmain_end
	v_and_b32_e32 v2, 31, v0
	v_lshlrev_b32_e32 v3, 5, v0
	v_and_b32_e32 v3, 0xc00, v3
	v_lshl_or_b32 v8, v2, 2, v3
	v_add_u32_e32 v8, 0xb800, v8
	ds_read2_b32 v[2:3], v8 offset1:32
	ds_read2_b32 v[4:5], v8 offset0:64 offset1:96
	ds_read2_b32 v[6:7], v8 offset0:128 offset1:160
	ds_read2_b32 v[10:11], v8 offset0:192 offset1:224
	s_mov_b32 s8, 0xf800000
	s_lshr_b32 s2, s30, 3
	s_lshl_b32 s2, s2, 7
	s_add_u32 s2, s2, 0x300000
	s_add_u32 s6, s6, s2
	s_addc_u32 s7, s7, 0
	s_mov_b32 s4, 0
	s_mov_b32 s5, 0x41d00000
	s_mov_b32 s16, 0
	s_mov_b32 s17, 0x420e0000
	s_waitcnt lgkmcnt(0)
	v_min3_f32 v2, v2, v3, v4
	v_min3_f32 v5, v5, v6, v7
	v_min3_f32 v2, v2, v10, v11
	v_min_f32_e32 v2, v2, v5
	s_waitcnt lgkmcnt(0)
	v_add_f32_e32 v20, v20, v21
	v_add_f32_e32 v22, v22, v23
	v_add_f32_e32 v24, v24, v25
	v_add_f32_e32 v26, v26, v27
	v_add_f32_e32 v28, v28, v29
	v_add_f32_e32 v30, v30, v31
	v_add_f32_e32 v32, v32, v33
	v_add_f32_e32 v34, v34, v35
	v_add_f32_e32 v20, v20, v22
	v_add_f32_e32 v24, v24, v26
	v_add_f32_e32 v28, v28, v30
	v_add_f32_e32 v32, v32, v34
	v_add_f32_e32 v20, v20, v24
	v_add_f32_e32 v28, v28, v32
	v_add_f32_e32 v20, v20, v28
	v_add_f32_e32 v2, v2, v20
	v_max_f32_e32 v2, 0, v2
	v_mul_f32_e32 v3, 0x4f800000, v2
	v_cmp_gt_f32_e32 vcc, s8, v2
	s_nop 1
	v_cndmask_b32_e32 v2, v2, v3, vcc
	v_sqrt_f32_e32 v3, v2
	s_nop 0
	v_add_u32_e32 v4, -1, v3
	v_fma_f32 v5, -v4, v3, v2
	v_cmp_ge_f32_e64 s[18:19], 0, v5
	v_add_u32_e32 v5, 1, v3
	s_nop 0
	v_cndmask_b32_e64 v4, v3, v4, s[18:19]
	v_fma_f32 v3, -v5, v3, v2
	v_cmp_lt_f32_e64 s[18:19], 0, v3
	s_nop 1
	v_cndmask_b32_e64 v3, v4, v5, s[18:19]
	v_mul_f32_e32 v4, 0x37800000, v3
	v_cndmask_b32_e32 v3, v3, v4, vcc
	v_mov_b32_e32 v4, 0x260
	v_cmp_class_f32_e32 vcc, v2, v4
	s_nop 1
	v_cndmask_b32_e32 v2, v3, v2, vcc
	s_nop 1
	v_add_f32_dpp v3, v2, v2 quad_perm:[1,0,3,2] row_mask:0xf bank_mask:0xf
	s_nop 1
	v_add_f32_dpp v4, v3, v3 quad_perm:[2,3,0,1] row_mask:0xf bank_mask:0xf
	s_nop 1
	v_add_f32_dpp v5, v4, v4 row_half_mirror row_mask:0xf bank_mask:0xf
	s_nop 1
	v_add_f32_dpp v6, v5, v5 row_mirror row_mask:0xf bank_mask:0xf
	s_nop 1
	v_readlane_b32 s12, v6, 0
	v_readlane_b32 s13, v6, 16
	v_readlane_b32 s14, v6, 32
	v_readlane_b32 s15, v6, 48
	s_nop 3
	v_mov_b32_e32 v7, s12
	v_add_f32_e32 v7, s13, v7
	v_mov_b32_e32 v9, s14
	v_add_f32_e32 v9, s15, v9
	v_add_f32_e32 v0, v7, v9
	v_mov_b32_e32 v4, 0
	s_mov_b64 exec, 1
	v_cvt_f64_f32_e32 v[6:7], v0
	v_add_f64 v[8:9], v[6:7], s[4:5]
	global_atomic_add_f64 v[10:11], v4, v[8:9], s[6:7] sc0
	s_waitcnt vmcnt(0)
	v_cmp_le_f64_e32 vcc, s[16:17], v[10:11]
	s_and_saveexec_b64 s[2:3], vcc
	s_cbranch_execz .Lmain_end
	v_add_f64 v[10:11], v[10:11], -s[16:17]
	v_add_f64 v[10:11], v[10:11], v[6:7]
	v_cvt_f32_f64_e32 v0, v[10:11]
	v_mul_f32_e32 v0, 0x38000000, v0
	global_atomic_add_f32 v4, v0, s[10:11]
